# stream: barrier moved up so only 3 loads per wave are issued before the partial-u hand-off (smaller initial burst); rotated wave-row kept
# speedup vs baseline: 1.0291x; 1.0075x over previous
.LBB1_2:
	s_or_b64 exec, exec, s[0:1]
	s_lshr_b32 s8, s3, 6
	s_add_i32 s8, s8, s2
	s_and_b32 s8, s8, 15
	s_lshl_b32 s0, s2, 7
	v_and_b32_e32 v24, 63, v0
	s_add_i32 s9, s8, s0
	s_waitcnt lgkmcnt(0)
	s_and_b32 s1, s5, 0xffff
	s_mov_b32 s3, 0x20000
	s_brev_b32 s2, 16
	s_mov_b32 s0, s4
	v_lshlrev_b32_e32 v25, 4, v24
	s_lshl_b32 s4, s9, 12
	buffer_load_dwordx4 v[26:29], v25, s[0:3], s4 offen offset:1024 nt
	buffer_load_dwordx4 v[30:33], v25, s[0:3], s4 offen nt
	buffer_load_dwordx4 v[34:37], v25, s[0:3], s4 offen offset:2048 nt
	s_barrier
	s_add_i32 s5, s4, 0x10000
	buffer_load_dwordx4 v[38:41], v25, s[0:3], s5 offen offset:1024 nt
	buffer_load_dwordx4 v[42:45], v25, s[0:3], s5 offen nt
	buffer_load_dwordx4 v[16:19], v25, s[0:3], s4 offen offset:3072 nt
	s_add_i32 s10, s4, 0x20000
	buffer_load_dwordx4 v[46:49], v25, s[0:3], s5 offen offset:2048 nt
	buffer_load_dwordx4 v[20:23], v25, s[0:3], s5 offen offset:3072 nt
	buffer_load_dwordx4 v[50:53], v25, s[0:3], s10 offen offset:1024 nt
	buffer_load_dwordx4 v[54:57], v25, s[0:3], s10 offen nt
	ds_read_b128 v[4:7], v25 offset:1024
	ds_read_b128 v[0:3], v25
	ds_read_b128 v[12:15], v25 offset:2048
	ds_read_b128 v[8:11], v25 offset:3072
	s_add_i32 s5, s4, 0x30000
	v_cmp_gt_u32_e32 vcc, 8, v24
	s_waitcnt vmcnt(9) lgkmcnt(3)
	v_pk_mul_f32 v[28:29], v[6:7], v[28:29]
	v_pk_mul_f32 v[26:27], v[4:5], v[26:27]
	s_waitcnt vmcnt(8) lgkmcnt(2)
	v_pk_fma_f32 v[32:33], v[2:3], v[32:33], v[28:29]
	v_pk_fma_f32 v[30:31], v[0:1], v[30:31], v[26:27]
	buffer_load_dwordx4 v[26:29], v25, s[0:3], s5 offen offset:1024 nt
	s_waitcnt vmcnt(8) lgkmcnt(1)
	v_pk_fma_f32 v[58:59], v[14:15], v[36:37], v[32:33]
	v_pk_fma_f32 v[60:61], v[12:13], v[34:35], v[30:31]
	buffer_load_dwordx4 v[30:33], v25, s[0:3], s5 offen nt
	s_waitcnt vmcnt(8)
	v_pk_mul_f32 v[34:35], v[6:7], v[40:41]
	v_pk_mul_f32 v[36:37], v[4:5], v[38:39]
	s_waitcnt vmcnt(7)
	v_pk_fma_f32 v[44:45], v[2:3], v[44:45], v[34:35]
	v_pk_fma_f32 v[42:43], v[0:1], v[42:43], v[36:37]
	buffer_load_dwordx4 v[34:37], v25, s[0:3], s10 offen offset:2048 nt
	s_waitcnt vmcnt(4)
	v_pk_mul_f32 v[38:39], v[6:7], v[52:53]
	v_pk_mul_f32 v[40:41], v[4:5], v[50:51]
	s_waitcnt vmcnt(3)
	v_pk_fma_f32 v[50:51], v[2:3], v[56:57], v[38:39]
	v_pk_fma_f32 v[52:53], v[0:1], v[54:55], v[40:41]
	buffer_load_dwordx4 v[38:41], v25, s[0:3], s10 offen offset:3072 nt
	v_pk_fma_f32 v[48:49], v[14:15], v[48:49], v[44:45]
	v_pk_fma_f32 v[46:47], v[12:13], v[46:47], v[42:43]
	s_waitcnt lgkmcnt(0)
	v_pk_fma_f32 v[18:19], v[10:11], v[18:19], v[58:59]
	v_pk_fma_f32 v[16:17], v[8:9], v[16:17], v[60:61]
	v_add_f32_e32 v61, v18, v19
	v_add_f32_e32 v60, v16, v17
	v_pk_fma_f32 v[16:17], v[10:11], v[22:23], v[48:49]
	v_pk_fma_f32 v[18:19], v[8:9], v[20:21], v[46:47]
	v_add_f32_e32 v16, v16, v17
	v_add_f32_e32 v18, v18, v19
	v_add_f32_e32 v60, v60, v61
	v_add_f32_e32 v16, v18, v16
	s_add_i32 s10, s4, 0x50000
	s_waitcnt vmcnt(3)
	v_pk_mul_f32 v[28:29], v[6:7], v[28:29]
	v_pk_mul_f32 v[26:27], v[4:5], v[26:27]
	v_add_f32_dpp v16, v16, v16 quad_perm:[1,0,3,2] row_mask:0xf bank_mask:0xf bound_ctrl:1
	s_waitcnt vmcnt(2)
	v_pk_fma_f32 v[54:55], v[2:3], v[32:33], v[28:29]
	v_pk_fma_f32 v[56:57], v[0:1], v[30:31], v[26:27]
	buffer_load_dwordx4 v[26:29], v25, s[0:3], s5 offen offset:2048 nt
	buffer_load_dwordx4 v[30:33], v25, s[0:3], s5 offen offset:3072 nt
	s_add_i32 s5, s4, 0x40000
	buffer_load_dwordx4 v[42:45], v25, s[0:3], s5 offen offset:1024 nt
	s_waitcnt vmcnt(4)
	v_pk_fma_f32 v[50:51], v[14:15], v[36:37], v[50:51]
	v_pk_fma_f32 v[52:53], v[12:13], v[34:35], v[52:53]
	buffer_load_dwordx4 v[34:37], v25, s[0:3], s5 offen nt
	v_add_f32_dpp v16, v16, v16 quad_perm:[2,3,0,1] row_mask:0xf bank_mask:0xf bound_ctrl:1
	s_waitcnt vmcnt(4)
	v_pk_fma_f32 v[58:59], v[10:11], v[40:41], v[50:51]
	v_pk_fma_f32 v[38:39], v[8:9], v[38:39], v[52:53]
	v_add_f32_e32 v19, v58, v59
	v_add_f32_e32 v17, v38, v39
	v_add_f32_dpp v58, v60, v60 quad_perm:[1,0,3,2] row_mask:0xf bank_mask:0xf bound_ctrl:1
	v_add_f32_e32 v18, v17, v19
	v_add_f32_dpp v16, v16, v16 row_ror:4 row_mask:0xf bank_mask:0xf bound_ctrl:1
	v_add_f32_dpp v17, v58, v58 quad_perm:[2,3,0,1] row_mask:0xf bank_mask:0xf bound_ctrl:1
	buffer_load_dwordx4 v[20:23], v25, s[0:3], s5 offen offset:2048 nt
	buffer_load_dwordx4 v[46:49], v25, s[0:3], s5 offen offset:3072 nt
	v_add_f32_dpp v17, v17, v17 row_ror:4 row_mask:0xf bank_mask:0xf bound_ctrl:1
	v_add_f32_dpp v58, v16, v16 row_ror:8 row_mask:0xf bank_mask:0xf bound_ctrl:1
	buffer_load_dwordx4 v[38:41], v25, s[0:3], s10 offen nt
	buffer_load_dwordx4 v[50:53], v25, s[0:3], s10 offen offset:1024 nt
	v_add_f32_dpp v17, v17, v17 row_ror:8 row_mask:0xf bank_mask:0xf bound_ctrl:1
	v_mov_b32_e32 v19, v17
	v_mov_b32_e32 v59, v58
	s_nop 0
	v_permlane16_swap_b32_e32 v17, v19
	v_permlane16_swap_b32_e32 v58, v59
	v_add_f32_e32 v16, v17, v19
	v_add_f32_e32 v17, v58, v59
	s_add_i32 s5, s4, 0x60000
	s_add_i32 s4, s4, 0x70000
	v_add_f32_dpp v18, v18, v18 quad_perm:[1,0,3,2] row_mask:0xf bank_mask:0xf bound_ctrl:1
	s_waitcnt vmcnt(7)
	v_pk_fma_f32 v[28:29], v[14:15], v[28:29], v[54:55]
	v_pk_fma_f32 v[54:55], v[12:13], v[26:27], v[56:57]
	s_waitcnt vmcnt(6)
	v_pk_fma_f32 v[58:59], v[10:11], v[32:33], v[28:29]
	buffer_load_dwordx4 v[26:29], v25, s[0:3], s10 offen offset:2048 nt
	v_pk_fma_f32 v[54:55], v[8:9], v[30:31], v[54:55]
	buffer_load_dwordx4 v[30:33], v25, s[0:3], s10 offen offset:3072 nt
	v_add_f32_e32 v66, v54, v55
	s_waitcnt vmcnt(7)
	v_pk_mul_f32 v[54:55], v[6:7], v[44:45]
	v_pk_mul_f32 v[56:57], v[4:5], v[42:43]
	buffer_load_dwordx4 v[42:45], v25, s[0:3], s5 offen offset:1024 nt
	s_waitcnt vmcnt(7)
	v_pk_fma_f32 v[54:55], v[2:3], v[36:37], v[54:55]
	v_pk_fma_f32 v[56:57], v[0:1], v[34:35], v[56:57]
	buffer_load_dwordx4 v[34:37], v25, s[0:3], s5 offen nt
	v_add_f32_dpp v18, v18, v18 quad_perm:[2,3,0,1] row_mask:0xf bank_mask:0xf bound_ctrl:1
	s_waitcnt vmcnt(7)
	v_pk_fma_f32 v[22:23], v[14:15], v[22:23], v[54:55]
	v_pk_fma_f32 v[20:21], v[12:13], v[20:21], v[56:57]
	s_waitcnt vmcnt(6)
	v_pk_fma_f32 v[60:61], v[10:11], v[48:49], v[22:23]
	v_pk_fma_f32 v[22:23], v[8:9], v[46:47], v[20:21]
	s_waitcnt vmcnt(4)
	v_pk_mul_f32 v[54:55], v[4:5], v[50:51]
	v_pk_mul_f32 v[20:21], v[6:7], v[52:53]
	v_pk_fma_f32 v[38:39], v[0:1], v[38:39], v[54:55]
	buffer_load_dwordx4 v[46:49], v25, s[0:3], s5 offen offset:2048 nt
	buffer_load_dwordx4 v[50:53], v25, s[0:3], s5 offen offset:3072 nt
	v_pk_fma_f32 v[20:21], v[2:3], v[40:41], v[20:21]
	v_add_f32_e32 v23, v22, v23
	v_add_f32_dpp v18, v18, v18 row_ror:4 row_mask:0xf bank_mask:0xf bound_ctrl:1
	s_waitcnt vmcnt(5)
	v_pk_fma_f32 v[26:27], v[12:13], v[26:27], v[38:39]
	buffer_load_dwordx4 v[38:41], v25, s[0:3], s4 offen nt
	buffer_load_dwordx4 v[54:57], v25, s[0:3], s4 offen offset:1024 nt
	v_pk_fma_f32 v[20:21], v[14:15], v[28:29], v[20:21]
	s_waitcnt vmcnt(6)
	v_pk_fma_f32 v[30:31], v[8:9], v[30:31], v[26:27]
	v_pk_fma_f32 v[62:63], v[10:11], v[32:33], v[20:21]
	v_add_f32_dpp v18, v18, v18 row_ror:8 row_mask:0xf bank_mask:0xf bound_ctrl:1
	s_waitcnt vmcnt(5)
	v_pk_mul_f32 v[20:21], v[6:7], v[44:45]
	v_pk_mul_f32 v[26:27], v[4:5], v[42:43]
	buffer_load_dwordx4 v[42:45], v25, s[0:3], s4 offen offset:2048 nt
	s_waitcnt vmcnt(5)
	v_pk_fma_f32 v[64:65], v[0:1], v[34:35], v[26:27]
	buffer_load_dwordx4 v[32:35], v25, s[0:3], s4 offen offset:3072 nt
	v_add_f32_e32 v27, v60, v61
	v_add_f32_e32 v23, v23, v27
	v_pk_fma_f32 v[36:37], v[2:3], v[36:37], v[20:21]
	v_add_f32_e32 v20, v58, v59
	v_add_f32_dpp v23, v23, v23 quad_perm:[1,0,3,2] row_mask:0xf bank_mask:0xf bound_ctrl:1
	v_add_f32_e32 v20, v66, v20
	v_mov_b32_e32 v19, v18
	v_add_f32_dpp v23, v23, v23 quad_perm:[2,3,0,1] row_mask:0xf bank_mask:0xf bound_ctrl:1
	v_add_f32_dpp v20, v20, v20 quad_perm:[1,0,3,2] row_mask:0xf bank_mask:0xf bound_ctrl:1
	v_permlane16_swap_b32_e32 v18, v19
	v_add_f32_dpp v23, v23, v23 row_ror:4 row_mask:0xf bank_mask:0xf bound_ctrl:1
	v_add_f32_dpp v20, v20, v20 quad_perm:[2,3,0,1] row_mask:0xf bank_mask:0xf bound_ctrl:1
	v_add_f32_e32 v18, v18, v19
	v_add_f32_dpp v23, v23, v23 row_ror:8 row_mask:0xf bank_mask:0xf bound_ctrl:1
	v_mov_b32_e32 v27, v23
	s_nop 1
	v_permlane16_swap_b32_e32 v23, v27
	v_add_f32_e32 v28, v23, v27
	v_add_f32_e32 v23, v30, v31
	s_waitcnt vmcnt(5)
	v_pk_fma_f32 v[30:31], v[14:15], v[48:49], v[36:37]
	v_pk_fma_f32 v[36:37], v[12:13], v[46:47], v[64:65]
	s_waitcnt vmcnt(4)
	v_pk_fma_f32 v[30:31], v[10:11], v[52:53], v[30:31]
	v_pk_fma_f32 v[36:37], v[8:9], v[50:51], v[36:37]
	v_add_f32_e32 v27, v62, v63
	v_add_f32_e32 v36, v36, v37
	v_add_f32_e32 v30, v30, v31
	v_add_f32_e32 v23, v23, v27
	v_add_f32_e32 v30, v36, v30
	v_add_f32_dpp v20, v20, v20 row_ror:4 row_mask:0xf bank_mask:0xf bound_ctrl:1
	v_add_f32_dpp v23, v23, v23 quad_perm:[1,0,3,2] row_mask:0xf bank_mask:0xf bound_ctrl:1
	v_add_f32_dpp v30, v30, v30 quad_perm:[1,0,3,2] row_mask:0xf bank_mask:0xf bound_ctrl:1
	v_add_f32_dpp v20, v20, v20 row_ror:8 row_mask:0xf bank_mask:0xf bound_ctrl:1
	v_add_f32_dpp v23, v23, v23 quad_perm:[2,3,0,1] row_mask:0xf bank_mask:0xf bound_ctrl:1
	v_add_f32_dpp v30, v30, v30 quad_perm:[2,3,0,1] row_mask:0xf bank_mask:0xf bound_ctrl:1
	v_mov_b32_e32 v21, v20
	v_add_f32_dpp v23, v23, v23 row_ror:4 row_mask:0xf bank_mask:0xf bound_ctrl:1
	v_add_f32_dpp v30, v30, v30 row_ror:4 row_mask:0xf bank_mask:0xf bound_ctrl:1
	v_permlane16_swap_b32_e32 v20, v21
	v_add_f32_dpp v23, v23, v23 row_ror:8 row_mask:0xf bank_mask:0xf bound_ctrl:1
	v_add_f32_dpp v30, v30, v30 row_ror:8 row_mask:0xf bank_mask:0xf bound_ctrl:1
	v_mov_b32_e32 v27, v23
	v_mov_b32_e32 v31, v30
	s_nop 0
	v_permlane16_swap_b32_e32 v23, v27
	v_permlane16_swap_b32_e32 v30, v31
	v_add_f32_e32 v21, v20, v21
	v_add_f32_e32 v23, v23, v27
	v_add_f32_e32 v30, v30, v31
	v_mov_b32_e32 v19, v16
	v_mov_b32_e32 v20, v17
	v_mov_b32_e32 v22, v18
	v_mov_b32_e32 v26, v21
	v_mov_b32_e32 v29, v28
	v_mov_b32_e32 v27, v23
	v_mov_b32_e32 v31, v30
	v_permlane32_swap_b32_e32 v16, v19
	v_permlane32_swap_b32_e32 v17, v20
	v_permlane32_swap_b32_e32 v18, v22
	v_permlane32_swap_b32_e32 v21, v26
	v_permlane32_swap_b32_e32 v28, v29
	v_permlane32_swap_b32_e32 v23, v27
	s_waitcnt vmcnt(2)
	v_pk_mul_f32 v[6:7], v[6:7], v[56:57]
	v_pk_mul_f32 v[4:5], v[4:5], v[54:55]
	v_pk_fma_f32 v[2:3], v[2:3], v[40:41], v[6:7]
	v_pk_fma_f32 v[0:1], v[0:1], v[38:39], v[4:5]
	v_permlane32_swap_b32_e32 v30, v31
	s_waitcnt vmcnt(1)
	v_pk_fma_f32 v[2:3], v[14:15], v[44:45], v[2:3]
	v_pk_fma_f32 v[0:1], v[12:13], v[42:43], v[0:1]
	s_waitcnt vmcnt(0)
	v_pk_fma_f32 v[2:3], v[10:11], v[34:35], v[2:3]
	v_pk_fma_f32 v[0:1], v[8:9], v[32:33], v[0:1]
	s_nop 0
	v_add_f32_e32 v0, v0, v1
	v_add_f32_e32 v1, v2, v3
	v_add_f32_e32 v0, v0, v1
	s_nop 1
	v_add_f32_dpp v0, v0, v0 quad_perm:[1,0,3,2] row_mask:0xf bank_mask:0xf bound_ctrl:1
	s_nop 1
	v_add_f32_dpp v0, v0, v0 quad_perm:[2,3,0,1] row_mask:0xf bank_mask:0xf bound_ctrl:1
	s_nop 1
	v_add_f32_dpp v0, v0, v0 row_ror:4 row_mask:0xf bank_mask:0xf bound_ctrl:1
	s_nop 1
	v_add_f32_dpp v0, v0, v0 row_ror:8 row_mask:0xf bank_mask:0xf bound_ctrl:1
	v_mov_b32_e32 v1, v0
	s_nop 1
	v_permlane16_swap_b32_e32 v0, v1
	v_add_f32_e32 v0, v0, v1
	v_mov_b32_e32 v1, v0
	s_nop 1
	v_permlane32_swap_b32_e32 v0, v1
	s_and_saveexec_b64 s[0:1], vcc
	s_cbranch_execz .LBB1_4
	v_add_f32_e32 v6, v16, v19
	v_cmp_eq_u32_e32 vcc, 0, v24
	v_add_f32_e32 v5, v17, v20
	v_add_f32_e32 v4, v18, v22
	v_cndmask_b32_e32 v6, 0, v6, vcc
	v_cmp_eq_u32_e32 vcc, 1, v24
	v_add_f32_e32 v3, v21, v26
	v_add_f32_e32 v2, v28, v29
	v_cndmask_b32_e32 v5, v6, v5, vcc
	v_cmp_eq_u32_e32 vcc, 2, v24
	v_add_f32_e32 v0, v0, v1
	v_add_f32_e32 v1, v30, v31
	v_cndmask_b32_e32 v4, v5, v4, vcc
	v_cmp_eq_u32_e32 vcc, 3, v24
	s_lshl_b32 s0, s8, 13
	s_and_b32 s0, s0, 0x1e000
	v_cndmask_b32_e32 v3, v4, v3, vcc
	v_cmp_eq_u32_e32 vcc, 4, v24
	s_add_u32 s0, s6, s0
	s_addc_u32 s1, s7, 0
	v_cndmask_b32_e32 v2, v3, v2, vcc
	v_add_f32_e32 v3, v23, v27
	v_cmp_eq_u32_e32 vcc, 5, v24
	s_nop 1
	v_cndmask_b32_e32 v2, v2, v3, vcc
	v_cmp_eq_u32_e32 vcc, 6, v24
	s_nop 1
	v_cndmask_b32_e32 v1, v2, v1, vcc
	v_cmp_eq_u32_e32 vcc, 7, v24
	s_nop 1
	v_cndmask_b32_e32 v2, v1, v0, vcc
	v_add_u32_e32 v0, s9, v25
	v_ashrrev_i32_e32 v0, 4, v0
	v_ashrrev_i32_e32 v1, 31, v0
	v_lshl_add_u64 v[0:1], v[0:1], 2, s[0:1]
	v_add_co_u32_e32 v0, vcc, 0x6000, v0
	s_nop 1
	v_addc_co_u32_e32 v1, vcc, 0, v1, vcc
	global_store_dword v[0:1], v2, off offset:64
